# dense SwiGLU-up GEMM: L2 prefetch of K-tile t+4 by dword LDS-DMA loads into a scratch LDS slot, 16 lines per wave, rows split over the workgroups that share a tile
# baseline (speedup 1.0000x reference)
.LBB0_564:
	v_mbcnt_lo_u32_b32 v252, -1, 0
	v_mbcnt_hi_u32_b32 v252, -1, v252
	v_and_b32_e32 v252, 15, v252
	v_mov_b32_e32 v253, s101
	v_and_b32_e32 v253, 3, v253
	v_lshl_add_u32 v252, v253, 4, v252
	v_mov_b32_e32 v253, s87
	v_lshrrev_b32_e32 v253, 3, v253
	v_cmp_ne_u32_e64 vcc, s100, 0
	s_nop 1
	v_lshrrev_b32_e32 v251, 2, v253
	v_cndmask_b32_e32 v253, v251, v253, vcc
	v_and_b32_e32 v253, 3, v253
	v_lshl_add_u32 v252, v253, 6, v252
	v_mul_u32_u24_e32 v252, 0x1000, v252
	s_cmp_lt_i32 s90, 8
	s_cselect_b64 s[0:1], -1, 0
	s_cmp_gt_i32 s91, 7
	s_cselect_b64 s[2:3], -1, 0
	s_and_b64 s[0:1], s[0:1], s[2:3]
	s_andn2_b64 vcc, exec, s[0:1]
	s_cbranch_vccnz .LBB0_581
	s_cmpk_gt_i32 s87, 0xabf
	v_readfirstlane_b32 s5, v0
	s_cbranch_scc1 .LBB0_581
	v_lshrrev_b32_e32 v1, 5, v0
	s_waitcnt lgkmcnt(0)
	v_lshrrev_b32_e32 v3, 1, v0
	v_and_b32_e32 v1, 4, v1
	v_bfe_u32 v2, v0, 2, 2
	s_waitcnt vmcnt(6)
	v_and_b32_e32 v13, 24, v3
	s_add_u32 s28, s58, 0x59680000
	v_or3_b32 v1, v1, v2, v13
	v_lshlrev_b32_e32 v2, 4, v0
	s_addc_u32 s29, s59, 0
	v_or_b32_e32 v10, 0x2000, v2
	s_add_u32 s30, s58, 0x2200000
	v_lshrrev_b32_e32 v3, 7, v10
	s_movk_i32 s2, 0x60
	s_addc_u32 s31, s59, 0
	v_and_or_b32 v4, v3, s2, v1
	s_waitcnt vmcnt(5)
	v_bfe_u32 v14, v0, 2, 4
	s_movk_i32 s2, 0x70
	s_ashr_i32 s34, s87, 31
	v_and_or_b32 v3, v3, s2, v14
	s_lshr_b32 s2, s34, 29
	s_add_i32 s2, s87, s2
	s_lshr_b32 s8, s5, 6
	s_ashr_i32 s3, s2, 3
	s_and_b32 s2, s2, -8
	s_lshr_b32 s10, s5, 8
	s_lshl_b32 s33, s8, 10
	s_sub_i32 s2, s87, s2
	s_cmp_lt_i32 s2, 0
	s_movk_i32 s35, 0x159
	s_cselect_b32 s4, s35, 0x158
	s_mul_i32 s2, s2, s4
	s_add_i32 s2, s2, s3
	s_mul_hi_i32 s3, s2, 0x2fa0be83
	s_lshr_b32 s4, s3, 31
	s_ashr_i32 s3, s3, 5
	s_add_i32 s3, s3, s4
	s_lshl_b32 s6, s3, 2
	s_mulk_i32 s3, 0xac
	s_sub_i32 s2, s2, s3
	s_bfe_u32 s3, s2, 0x2001d
	s_add_i32 s3, s2, s3
	s_sext_i32_i16 s4, s3
	s_and_b32 s3, s3, 0xfffc
	s_sub_i32 s2, s2, s3
	s_sext_i32_i16 s2, s2
	v_and_b32_e32 v5, 32, v0
	s_lshr_b32 s4, s4, 2
	s_add_i32 s20, s6, s2
	v_bitop3_b32 v11, v2, v5, 48 bitop3:0x6c
	v_and_b32_e32 v12, 64, v0
	s_ashr_i32 s21, s20, 31
	s_bfe_i64 s[6:7], s[4:5], 0x100000
	v_or_b32_e32 v2, v11, v12
	s_lshl_b64 s[2:3], s[20:21], 20
	s_lshl_b64 s[6:7], s[6:7], 20
	v_lshl_or_b32 v132, v3, 12, v2
	v_lshrrev_b32_e32 v3, 3, v0
	s_add_u32 s24, s30, s6
	v_and_or_b32 v1, v3, 32, v1
	s_addc_u32 s25, s31, s7
	s_add_i32 s21, s33, 0
	v_lshl_or_b32 v134, v1, 12, v2
	s_add_i32 m0, s21, 0x10000
	v_lshl_or_b32 v130, v4, 12, v2
	global_load_lds_dwordx4 v134, s[24:25]
	s_add_i32 m0, s21, 0x12000
	s_add_u32 s6, s24, 0x80000
	global_load_lds_dwordx4 v130, s[24:25]
	s_addc_u32 s7, s25, 0
	s_add_i32 m0, s21, 0x14000
	v_and_or_b32 v1, v3, 48, v14
	global_load_lds_dwordx4 v134, s[6:7]
	s_add_i32 m0, s21, 0x16000
	s_add_u32 s22, s28, s2
	s_addc_u32 s23, s29, s3
	s_add_i32 s36, s21, 0x2000
	v_lshl_or_b32 v136, v1, 12, v2
	global_load_lds_dwordx4 v130, s[6:7]
	s_mov_b32 m0, s21
	s_add_u32 s2, s22, 0x80000
	global_load_lds_dwordx4 v136, s[22:23]
	s_mov_b32 m0, s36
	s_addc_u32 s3, s23, 0
	s_add_i32 s37, s21, 0x4000
	global_load_lds_dwordx4 v132, s[22:23]
	s_mov_b32 m0, s37
	s_add_i32 s42, s21, 0x6000
	global_load_lds_dwordx4 v136, s[2:3]
	s_mov_b32 m0, s42
	v_mov_b32_e32 v135, 0
	global_load_lds_dwordx4 v132, s[2:3]
	v_mov_b32_e32 v131, v135
	v_mov_b32_e32 v137, v135
	v_mov_b32_e32 v133, v135
	s_cmp_eq_u32 s10, 1
	s_mov_b32 s43, 0
	v_lshl_add_u64 v[8:9], s[24:25], 0, v[134:135]
	v_lshl_add_u64 v[6:7], s[24:25], 0, v[130:131]
	v_lshl_add_u64 v[2:3], s[22:23], 0, v[136:137]
	s_cselect_b64 s[2:3], -1, 0
	s_cmp_lg_u32 s10, 1
	v_lshl_add_u64 v[4:5], s[22:23], 0, v[132:133]
	s_cbranch_scc1 .LBB0_568
	s_barrier

.LBB0_574:
	ds_read_b128 v[146:149], v152
	ds_read_b128 v[156:159], v152 offset:1024
	ds_read_b128 v[160:163], v152 offset:2048
	ds_read_b128 v[164:167], v152 offset:3072
	ds_read_b128 v[168:171], v153
	ds_read_b128 v[172:175], v153 offset:1024
	ds_read_b128 v[176:179], v153 offset:2048
	ds_read_b128 v[180:183], v153 offset:3072
	s_add_u32 s24, s22, 0xfff80080
	s_addc_u32 s25, s23, -1
	s_cmp_eq_u32 s69, 28
	s_cselect_b32 s27, s15, s25
	s_cselect_b32 s26, s65, s24
	s_cselect_b32 s25, s13, s68
	s_cselect_b32 s24, s66, s67
	v_lshl_add_u64 v[216:217], s[22:23], 0, v[138:139]
	s_add_i32 m0, s21, 0xc000
	ds_read_b128 v[184:187], v154
	ds_read_b128 v[188:191], v154 offset:1024
	ds_read_b128 v[192:195], v154 offset:2048
	ds_read_b128 v[196:199], v154 offset:3072
	ds_read_b128 v[200:203], v154 offset:4096
	ds_read_b128 v[204:207], v154 offset:5120
	ds_read_b128 v[208:211], v154 offset:6144
	ds_read_b128 v[212:215], v154 offset:7168
	global_load_lds_dwordx4 v[216:217], off
	v_lshl_add_u64 v[216:217], s[22:23], 0, v[140:141]
	s_add_i32 m0, s21, 0xe000
	s_nop 0
	global_load_lds_dwordx4 v[216:217], off
	s_waitcnt vmcnt(8)
	s_waitcnt lgkmcnt(0)
	s_barrier
	s_setprio 1
	s_waitcnt lgkmcnt(0)
	v_mfma_f32_16x16x32_bf16 v[126:129], v[146:149], v[184:187], v[126:129]
	v_mfma_f32_16x16x32_bf16 v[122:125], v[160:163], v[184:187], v[122:125]
	v_mfma_f32_16x16x32_bf16 v[110:113], v[146:149], v[192:195], v[110:113]
	v_mfma_f32_16x16x32_bf16 v[106:109], v[160:163], v[192:195], v[106:109]
	v_mfma_f32_16x16x32_bf16 v[94:97], v[146:149], v[200:203], v[94:97]
	v_mfma_f32_16x16x32_bf16 v[90:93], v[160:163], v[200:203], v[90:93]
	v_mfma_f32_16x16x32_bf16 v[78:81], v[146:149], v[208:211], v[78:81]
	v_mfma_f32_16x16x32_bf16 v[74:77], v[160:163], v[208:211], v[74:77]
	v_mfma_f32_16x16x32_bf16 v[126:129], v[156:159], v[188:191], v[126:129]
	v_mfma_f32_16x16x32_bf16 v[122:125], v[164:167], v[188:191], v[122:125]
	v_mfma_f32_16x16x32_bf16 v[110:113], v[156:159], v[196:199], v[110:113]
	v_mfma_f32_16x16x32_bf16 v[106:109], v[164:167], v[196:199], v[106:109]
	v_mfma_f32_16x16x32_bf16 v[94:97], v[156:159], v[204:207], v[94:97]
	v_mfma_f32_16x16x32_bf16 v[90:93], v[164:167], v[204:207], v[90:93]
	v_mfma_f32_16x16x32_bf16 v[78:81], v[156:159], v[212:215], v[78:81]
	v_mfma_f32_16x16x32_bf16 v[74:77], v[164:167], v[212:215], v[74:77]
	s_setprio 0
	s_setprio 1
	v_mfma_f32_16x16x32_bf16 v[118:121], v[168:171], v[184:187], v[118:121]
	v_mfma_f32_16x16x32_bf16 v[114:117], v[176:179], v[184:187], v[114:117]
	v_mfma_f32_16x16x32_bf16 v[102:105], v[168:171], v[192:195], v[102:105]
	v_mfma_f32_16x16x32_bf16 v[98:101], v[176:179], v[192:195], v[98:101]
	v_mfma_f32_16x16x32_bf16 v[86:89], v[168:171], v[200:203], v[86:89]
	v_mfma_f32_16x16x32_bf16 v[82:85], v[176:179], v[200:203], v[82:85]
	v_mfma_f32_16x16x32_bf16 v[70:73], v[168:171], v[208:211], v[70:73]
	v_mfma_f32_16x16x32_bf16 v[66:69], v[176:179], v[208:211], v[66:69]
	v_mfma_f32_16x16x32_bf16 v[118:121], v[172:175], v[188:191], v[118:121]
	v_mfma_f32_16x16x32_bf16 v[114:117], v[180:183], v[188:191], v[114:117]
	v_mfma_f32_16x16x32_bf16 v[102:105], v[172:175], v[196:199], v[102:105]
	v_mfma_f32_16x16x32_bf16 v[98:101], v[180:183], v[196:199], v[98:101]
	v_mfma_f32_16x16x32_bf16 v[86:89], v[172:175], v[204:207], v[86:89]
	v_mfma_f32_16x16x32_bf16 v[82:85], v[180:183], v[204:207], v[82:85]
	v_mfma_f32_16x16x32_bf16 v[70:73], v[172:175], v[212:215], v[70:73]
	v_mfma_f32_16x16x32_bf16 v[66:69], v[180:183], v[212:215], v[66:69]
	s_setprio 0
	s_barrier
	s_add_i32 s70, s61, s33
	v_lshl_add_u64 v[216:217], s[24:25], 0, v[134:135]
	s_mov_b32 m0, s70
	ds_read_b128 v[184:187], v154 offset:16384
	ds_read_b128 v[188:191], v154 offset:17408
	ds_read_b128 v[192:195], v154 offset:18432
	ds_read_b128 v[196:199], v154 offset:19456
	ds_read_b128 v[200:203], v154 offset:20480
	ds_read_b128 v[204:207], v154 offset:21504
	ds_read_b128 v[208:211], v154 offset:22528
	ds_read_b128 v[212:215], v154 offset:23552
	global_load_lds_dwordx4 v[216:217], off
	s_add_i32 m0, s70, 0x2000
	s_add_u32 s70, s24, 0x80000
	v_lshl_add_u64 v[218:219], s[24:25], 0, v[130:131]
	s_addc_u32 s71, s25, 0
	s_add_i32 s72, s62, s33
	global_load_lds_dwordx4 v[218:219], off
	v_lshl_add_u64 v[220:221], s[70:71], 0, v[134:135]
	s_mov_b32 m0, s72
	v_lshl_add_u64 v[222:223], s[26:27], 0, v[132:133]
	global_load_lds_dwordx4 v[220:221], off
	v_lshl_add_u64 v[220:221], s[70:71], 0, v[130:131]
	s_add_i32 m0, s72, 0x2000
	s_nop 0
	global_load_lds_dwordx4 v[220:221], off
	v_lshl_add_u64 v[220:221], s[26:27], 0, v[136:137]
	s_mov_b32 m0, s21
	s_nop 0
	global_load_lds_dwordx4 v[220:221], off
	s_mov_b32 m0, s36
	s_nop 0
	global_load_lds_dwordx4 v[222:223], off
	s_cmp_lg_u32 s100, 0
	s_cselect_b32 s98, s24, s26
	s_cselect_b32 s99, s25, s27
	s_add_u32 s98, s98, 0x100
	s_addc_u32 s99, s99, 0
	s_mov_b32 m0, 0x21700
	s_nop 0
	global_load_lds_dword v252, s[98:99]
	s_add_u32 s98, s98, 0x80
	s_addc_u32 s99, s99, 0
	global_load_lds_dword v252, s[98:99]
	s_waitcnt vmcnt(10)
	s_waitcnt lgkmcnt(0)
	s_barrier
	s_setprio 1
	s_waitcnt lgkmcnt(0)
	v_mfma_f32_16x16x32_bf16 v[62:65], v[146:149], v[184:187], v[62:65]
	v_mfma_f32_16x16x32_bf16 v[58:61], v[160:163], v[184:187], v[58:61]
	v_mfma_f32_16x16x32_bf16 v[46:49], v[146:149], v[192:195], v[46:49]
	v_mfma_f32_16x16x32_bf16 v[42:45], v[160:163], v[192:195], v[42:45]
	v_mfma_f32_16x16x32_bf16 v[30:33], v[146:149], v[200:203], v[30:33]
	v_mfma_f32_16x16x32_bf16 v[26:29], v[160:163], v[200:203], v[26:29]
	v_mfma_f32_16x16x32_bf16 v[14:17], v[146:149], v[208:211], v[14:17]
	v_mfma_f32_16x16x32_bf16 v[10:13], v[160:163], v[208:211], v[10:13]
	v_mfma_f32_16x16x32_bf16 v[62:65], v[156:159], v[188:191], v[62:65]
	v_mfma_f32_16x16x32_bf16 v[58:61], v[164:167], v[188:191], v[58:61]
	v_mfma_f32_16x16x32_bf16 v[46:49], v[156:159], v[196:199], v[46:49]
	v_mfma_f32_16x16x32_bf16 v[42:45], v[164:167], v[196:199], v[42:45]
	v_mfma_f32_16x16x32_bf16 v[30:33], v[156:159], v[204:207], v[30:33]
	v_mfma_f32_16x16x32_bf16 v[26:29], v[164:167], v[204:207], v[26:29]
	v_mfma_f32_16x16x32_bf16 v[14:17], v[156:159], v[212:215], v[14:17]
	v_mfma_f32_16x16x32_bf16 v[10:13], v[164:167], v[212:215], v[10:13]
	s_setprio 0
	s_setprio 1
	v_mfma_f32_16x16x32_bf16 v[54:57], v[168:171], v[184:187], v[54:57]
	v_mfma_f32_16x16x32_bf16 v[50:53], v[176:179], v[184:187], v[50:53]
	v_mfma_f32_16x16x32_bf16 v[38:41], v[168:171], v[192:195], v[38:41]
	v_mfma_f32_16x16x32_bf16 v[34:37], v[176:179], v[192:195], v[34:37]
	v_mfma_f32_16x16x32_bf16 v[22:25], v[168:171], v[200:203], v[22:25]
	v_mfma_f32_16x16x32_bf16 v[18:21], v[176:179], v[200:203], v[18:21]
	v_mfma_f32_16x16x32_bf16 v[6:9], v[168:171], v[208:211], v[6:9]
	v_mfma_f32_16x16x32_bf16 v[2:5], v[176:179], v[208:211], v[2:5]
	v_mfma_f32_16x16x32_bf16 v[54:57], v[172:175], v[188:191], v[54:57]
	v_mfma_f32_16x16x32_bf16 v[50:53], v[180:183], v[188:191], v[50:53]
	v_mfma_f32_16x16x32_bf16 v[38:41], v[172:175], v[196:199], v[38:41]
	v_mfma_f32_16x16x32_bf16 v[34:37], v[180:183], v[196:199], v[34:37]
	v_mfma_f32_16x16x32_bf16 v[22:25], v[172:175], v[204:207], v[22:25]
	v_mfma_f32_16x16x32_bf16 v[18:21], v[180:183], v[204:207], v[18:21]
	v_mfma_f32_16x16x32_bf16 v[6:9], v[172:175], v[212:215], v[6:9]
	v_mfma_f32_16x16x32_bf16 v[2:5], v[180:183], v[212:215], v[2:5]
	s_setprio 0
	s_barrier
	s_add_i32 s70, 0, 0x18000
	v_add_u32_e32 v155, s70, v150
	s_add_i32 s71, 0, 0x1c000
	ds_read_b128 v[146:149], v155
	ds_read_b128 v[156:159], v155 offset:1024
	ds_read_b128 v[160:163], v155 offset:2048
	ds_read_b128 v[164:167], v155 offset:3072
	v_add_u32_e32 v155, s71, v150
	ds_read_b128 v[168:171], v155
	ds_read_b128 v[172:175], v155 offset:1024
	ds_read_b128 v[176:179], v155 offset:2048
	ds_read_b128 v[180:183], v155 offset:3072
	s_add_u32 s26, s26, 0x80000
	s_addc_u32 s27, s27, 0
	s_mov_b32 m0, s37
	v_lshl_add_u64 v[224:225], s[26:27], 0, v[136:137]
	ds_read_b128 v[184:187], v154 offset:32768
	ds_read_b128 v[188:191], v154 offset:33792
	ds_read_b128 v[192:195], v154 offset:34816
	ds_read_b128 v[196:199], v154 offset:35840
	ds_read_b128 v[200:203], v154 offset:36864
	ds_read_b128 v[204:207], v154 offset:37888
	ds_read_b128 v[208:211], v154 offset:38912
	ds_read_b128 v[212:215], v154 offset:39936
	global_load_lds_dwordx4 v[224:225], off
	v_lshl_add_u64 v[224:225], s[26:27], 0, v[132:133]
	s_mov_b32 m0, s42
	s_nop 0
	global_load_lds_dwordx4 v[224:225], off
	s_waitcnt vmcnt(10)
	s_waitcnt lgkmcnt(0)
	s_barrier
	s_setprio 1
	s_waitcnt lgkmcnt(0)
	v_mfma_f32_16x16x32_bf16 v[126:129], v[146:149], v[184:187], v[126:129]
	v_mfma_f32_16x16x32_bf16 v[122:125], v[160:163], v[184:187], v[122:125]
	v_mfma_f32_16x16x32_bf16 v[110:113], v[146:149], v[192:195], v[110:113]
	v_mfma_f32_16x16x32_bf16 v[106:109], v[160:163], v[192:195], v[106:109]
	v_mfma_f32_16x16x32_bf16 v[94:97], v[146:149], v[200:203], v[94:97]
	v_mfma_f32_16x16x32_bf16 v[90:93], v[160:163], v[200:203], v[90:93]
	v_mfma_f32_16x16x32_bf16 v[78:81], v[146:149], v[208:211], v[78:81]
	v_mfma_f32_16x16x32_bf16 v[74:77], v[160:163], v[208:211], v[74:77]
	v_mfma_f32_16x16x32_bf16 v[126:129], v[156:159], v[188:191], v[126:129]
	v_mfma_f32_16x16x32_bf16 v[122:125], v[164:167], v[188:191], v[122:125]
	v_mfma_f32_16x16x32_bf16 v[110:113], v[156:159], v[196:199], v[110:113]
	v_mfma_f32_16x16x32_bf16 v[106:109], v[164:167], v[196:199], v[106:109]
	v_mfma_f32_16x16x32_bf16 v[94:97], v[156:159], v[204:207], v[94:97]
	v_mfma_f32_16x16x32_bf16 v[90:93], v[164:167], v[204:207], v[90:93]
	v_mfma_f32_16x16x32_bf16 v[78:81], v[156:159], v[212:215], v[78:81]
	v_mfma_f32_16x16x32_bf16 v[74:77], v[164:167], v[212:215], v[74:77]
	s_setprio 0
	s_setprio 1
	v_mfma_f32_16x16x32_bf16 v[118:121], v[168:171], v[184:187], v[118:121]
	v_mfma_f32_16x16x32_bf16 v[114:117], v[176:179], v[184:187], v[114:117]
	v_mfma_f32_16x16x32_bf16 v[102:105], v[168:171], v[192:195], v[102:105]
	v_mfma_f32_16x16x32_bf16 v[98:101], v[176:179], v[192:195], v[98:101]
	v_mfma_f32_16x16x32_bf16 v[86:89], v[168:171], v[200:203], v[86:89]
	v_mfma_f32_16x16x32_bf16 v[82:85], v[176:179], v[200:203], v[82:85]
	v_mfma_f32_16x16x32_bf16 v[70:73], v[168:171], v[208:211], v[70:73]
	v_mfma_f32_16x16x32_bf16 v[66:69], v[176:179], v[208:211], v[66:69]
	v_mfma_f32_16x16x32_bf16 v[118:121], v[172:175], v[188:191], v[118:121]
	v_mfma_f32_16x16x32_bf16 v[114:117], v[180:183], v[188:191], v[114:117]
	v_mfma_f32_16x16x32_bf16 v[102:105], v[172:175], v[196:199], v[102:105]
	v_mfma_f32_16x16x32_bf16 v[98:101], v[180:183], v[196:199], v[98:101]
	v_mfma_f32_16x16x32_bf16 v[86:89], v[172:175], v[204:207], v[86:89]
	v_mfma_f32_16x16x32_bf16 v[82:85], v[180:183], v[204:207], v[82:85]
	v_mfma_f32_16x16x32_bf16 v[70:73], v[172:175], v[212:215], v[70:73]
	v_mfma_f32_16x16x32_bf16 v[66:69], v[180:183], v[212:215], v[66:69]
	s_setprio 0
	s_barrier
	s_add_i32 s26, s70, s33
	v_lshl_add_u64 v[216:217], v[216:217], 0, s[8:9]
	s_mov_b32 m0, s26
	ds_read_b128 v[184:187], v154 offset:49152
	ds_read_b128 v[188:191], v154 offset:50176
	ds_read_b128 v[192:195], v154 offset:51200
	ds_read_b128 v[196:199], v154 offset:52224
	ds_read_b128 v[200:203], v154 offset:53248
	ds_read_b128 v[204:207], v154 offset:54272
	ds_read_b128 v[208:211], v154 offset:55296
	ds_read_b128 v[212:215], v154 offset:56320
	global_load_lds_dwordx4 v[216:217], off
	s_add_i32 m0, s26, 0x2000
	s_add_u32 s24, s24, 0x80080
	v_lshl_add_u64 v[216:217], v[218:219], 0, s[8:9]
	s_addc_u32 s25, s25, 0
	s_add_i32 s26, s71, s33
	global_load_lds_dwordx4 v[216:217], off
	v_lshl_add_u64 v[216:217], s[24:25], 0, v[134:135]
	s_mov_b32 m0, s26
	s_nop 0
	global_load_lds_dwordx4 v[216:217], off
	v_lshl_add_u64 v[216:217], s[24:25], 0, v[130:131]
	s_add_i32 m0, s26, 0x2000
	s_nop 0
	global_load_lds_dwordx4 v[216:217], off
	v_lshl_add_u64 v[216:217], v[220:221], 0, s[8:9]
	s_mov_b32 m0, s44
	s_nop 0
	global_load_lds_dwordx4 v[216:217], off
	v_lshl_add_u64 v[216:217], v[222:223], 0, s[8:9]
	s_mov_b32 m0, s45
	s_nop 0
	global_load_lds_dwordx4 v[216:217], off
	s_waitcnt vmcnt(10)
	s_waitcnt lgkmcnt(0)
	s_barrier
	s_setprio 1
	s_waitcnt lgkmcnt(0)
	v_mfma_f32_16x16x32_bf16 v[62:65], v[146:149], v[184:187], v[62:65]
	v_mfma_f32_16x16x32_bf16 v[58:61], v[160:163], v[184:187], v[58:61]
	v_mfma_f32_16x16x32_bf16 v[46:49], v[146:149], v[192:195], v[46:49]
	v_mfma_f32_16x16x32_bf16 v[42:45], v[160:163], v[192:195], v[42:45]
	v_mfma_f32_16x16x32_bf16 v[30:33], v[146:149], v[200:203], v[30:33]
	v_mfma_f32_16x16x32_bf16 v[26:29], v[160:163], v[200:203], v[26:29]
	v_mfma_f32_16x16x32_bf16 v[14:17], v[146:149], v[208:211], v[14:17]
	v_mfma_f32_16x16x32_bf16 v[10:13], v[160:163], v[208:211], v[10:13]
	v_mfma_f32_16x16x32_bf16 v[62:65], v[156:159], v[188:191], v[62:65]
	v_mfma_f32_16x16x32_bf16 v[58:61], v[164:167], v[188:191], v[58:61]
	v_mfma_f32_16x16x32_bf16 v[46:49], v[156:159], v[196:199], v[46:49]
	v_mfma_f32_16x16x32_bf16 v[42:45], v[164:167], v[196:199], v[42:45]
	v_mfma_f32_16x16x32_bf16 v[30:33], v[156:159], v[204:207], v[30:33]
	v_mfma_f32_16x16x32_bf16 v[26:29], v[164:167], v[204:207], v[26:29]
	v_mfma_f32_16x16x32_bf16 v[14:17], v[156:159], v[212:215], v[14:17]
	v_mfma_f32_16x16x32_bf16 v[10:13], v[164:167], v[212:215], v[10:13]
	s_setprio 0
	s_setprio 1
	v_mfma_f32_16x16x32_bf16 v[54:57], v[168:171], v[184:187], v[54:57]
	v_mfma_f32_16x16x32_bf16 v[50:53], v[176:179], v[184:187], v[50:53]
	v_mfma_f32_16x16x32_bf16 v[38:41], v[168:171], v[192:195], v[38:41]
	v_mfma_f32_16x16x32_bf16 v[34:37], v[176:179], v[192:195], v[34:37]
	v_mfma_f32_16x16x32_bf16 v[22:25], v[168:171], v[200:203], v[22:25]
	v_mfma_f32_16x16x32_bf16 v[18:21], v[176:179], v[200:203], v[18:21]
	v_mfma_f32_16x16x32_bf16 v[6:9], v[168:171], v[208:211], v[6:9]
	v_mfma_f32_16x16x32_bf16 v[2:5], v[176:179], v[208:211], v[2:5]
	v_mfma_f32_16x16x32_bf16 v[54:57], v[172:175], v[188:191], v[54:57]
	v_mfma_f32_16x16x32_bf16 v[50:53], v[180:183], v[188:191], v[50:53]
	v_mfma_f32_16x16x32_bf16 v[38:41], v[172:175], v[196:199], v[38:41]
	v_mfma_f32_16x16x32_bf16 v[34:37], v[180:183], v[196:199], v[34:37]
	v_mfma_f32_16x16x32_bf16 v[22:25], v[172:175], v[204:207], v[22:25]
	v_mfma_f32_16x16x32_bf16 v[18:21], v[180:183], v[204:207], v[18:21]
	v_mfma_f32_16x16x32_bf16 v[6:9], v[172:175], v[212:215], v[6:9]
	v_mfma_f32_16x16x32_bf16 v[2:5], v[180:183], v[212:215], v[2:5]
	s_setprio 0
	s_barrier
	s_add_i32 s69, s69, 2
	s_add_u32 s22, s22, 0x100
	s_addc_u32 s23, s23, 0
	s_add_u32 s67, s67, 0x100
	s_addc_u32 s68, s68, 0
	s_cmp_gt_u32 s69, 29
	s_cbranch_scc0 .LBB0_574
	s_and_b64 vcc, exec, s[10:11]
	s_cbranch_vccz .LBB0_577
	s_barrier
